# accumulator zeroing between GEMM units uses 64-bit register moves
# speedup vs baseline: 1.0074x; 1.0065x over previous
;     ...
; #pragma unroll
;         for (int a = 0; a < 2; ++a)
; #pragma unroll
;             for (int b = 0; b < 2; ++b)
; #pragma unroll
;                 for (int m = 0; m < 4; ++m)
; #pragma unroll
;                     for (int n = 0; n < 2; ++n) acc[a][b][m][n] = (f32x4){0.f, 0.f, 0.f, 0.f};
;         cur = nxt; cA = nA; cB = nB; ++ui; relax = ALIGN_EPI;
.LBB0_370:
	s_add_u32 s48, s2, 0x300000
	s_addc_u32 s49, s3, 0
	s_add_u32 s2, s4, 0x80
	s_addc_u32 s3, s5, 0
	v_mov_b32_e32 v48, 0
	v_lshl_add_u64 v[208:209], s[2:3], 0, v[204:205]
	v_lshl_add_u64 v[210:211], s[2:3], 0, v[206:207]
	s_mov_b32 s50, -2
	s_mov_b64 s[18:19], 0
	v_mov_b32_e32 v49, v48
	v_mov_b64_e32 v[0:1], v[48:49]
	v_mov_b64_e32 v[2:3], v[48:49]
	v_mov_b64_e32 v[4:5], v[48:49]
	v_mov_b64_e32 v[6:7], v[48:49]
	v_mov_b64_e32 v[8:9], v[48:49]
	v_mov_b64_e32 v[10:11], v[48:49]
	v_mov_b64_e32 v[12:13], v[48:49]
	v_mov_b64_e32 v[14:15], v[48:49]
	v_mov_b64_e32 v[16:17], v[48:49]
	v_mov_b64_e32 v[18:19], v[48:49]
	v_mov_b64_e32 v[20:21], v[48:49]
	v_mov_b64_e32 v[22:23], v[48:49]
	v_mov_b64_e32 v[32:33], v[48:49]
	v_mov_b64_e32 v[34:35], v[48:49]
	v_mov_b64_e32 v[36:37], v[48:49]
	v_mov_b64_e32 v[38:39], v[48:49]
	v_mov_b64_e32 v[50:51], v[48:49]
	v_mov_b64_e32 v[52:53], v[48:49]
	v_mov_b64_e32 v[54:55], v[48:49]
	v_mov_b64_e32 v[56:57], v[48:49]
	v_mov_b64_e32 v[58:59], v[48:49]
	v_mov_b64_e32 v[60:61], v[48:49]
	v_mov_b64_e32 v[62:63], v[48:49]
	v_mov_b64_e32 v[66:67], v[48:49]
	v_mov_b64_e32 v[68:69], v[48:49]
	v_mov_b64_e32 v[70:71], v[48:49]
	v_mov_b64_e32 v[72:73], v[48:49]
	v_mov_b64_e32 v[74:75], v[48:49]
	v_mov_b64_e32 v[76:77], v[48:49]
	v_mov_b64_e32 v[78:79], v[48:49]
	v_mov_b64_e32 v[80:81], v[48:49]
	v_mov_b64_e32 v[82:83], v[48:49]
	v_mov_b64_e32 v[84:85], v[48:49]
	v_mov_b64_e32 v[86:87], v[48:49]
	v_mov_b64_e32 v[88:89], v[48:49]
	v_mov_b64_e32 v[90:91], v[48:49]
	v_mov_b64_e32 v[92:93], v[48:49]
	v_mov_b64_e32 v[94:95], v[48:49]
	v_mov_b64_e32 v[96:97], v[48:49]
	v_mov_b64_e32 v[98:99], v[48:49]
	v_mov_b64_e32 v[100:101], v[48:49]
	v_mov_b64_e32 v[102:103], v[48:49]
	v_mov_b64_e32 v[104:105], v[48:49]
	v_mov_b64_e32 v[106:107], v[48:49]
	v_mov_b64_e32 v[108:109], v[48:49]
	v_mov_b64_e32 v[110:111], v[48:49]
	v_mov_b64_e32 v[112:113], v[48:49]
	v_mov_b64_e32 v[114:115], v[48:49]
	v_mov_b64_e32 v[116:117], v[48:49]
	v_mov_b64_e32 v[118:119], v[48:49]
	v_mov_b64_e32 v[120:121], v[48:49]
	v_mov_b64_e32 v[122:123], v[48:49]
	v_mov_b64_e32 v[124:125], v[48:49]
	v_mov_b64_e32 v[126:127], v[48:49]
	v_mov_b64_e32 v[128:129], v[48:49]
	v_mov_b64_e32 v[130:131], v[48:49]
	v_mov_b64_e32 v[132:133], v[48:49]
	v_mov_b64_e32 v[134:135], v[48:49]
	v_mov_b64_e32 v[136:137], v[48:49]
	v_mov_b64_e32 v[138:139], v[48:49]
	v_mov_b64_e32 v[140:141], v[48:49]
	v_mov_b64_e32 v[142:143], v[48:49]
	v_mov_b64_e32 v[144:145], v[48:49]
	s_branch .LBB0_372

;     ...
; #pragma unroll
;         for (int a = 0; a < 2; ++a)
; #pragma unroll
;             for (int b = 0; b < 2; ++b)
; #pragma unroll
;                 for (int m = 0; m < 4; ++m)
; #pragma unroll
;                     for (int n = 0; n < 2; ++n) acc[a][b][m][n] = (f32x4){0.f, 0.f, 0.f, 0.f};
;         cur = nxt; cA = nA; cB = nB; ++ui; relax = ALIGN_EPI;
.LBB0_622:
	s_add_u32 s48, s2, 0x300000
	s_addc_u32 s49, s3, 0
	s_add_u32 s2, s4, 0x80
	s_addc_u32 s3, s5, 0
	v_mov_b32_e32 v98, 0
	v_lshl_add_u64 v[208:209], s[2:3], 0, v[204:205]
	v_lshl_add_u64 v[210:211], s[2:3], 0, v[206:207]
	s_mov_b32 s50, -2
	s_mov_b64 s[16:17], 0
	v_mov_b32_e32 v99, v98
	v_mov_b64_e32 v[66:67], v[98:99]
	v_mov_b64_e32 v[68:69], v[98:99]
	v_mov_b64_e32 v[70:71], v[98:99]
	v_mov_b64_e32 v[72:73], v[98:99]
	v_mov_b64_e32 v[74:75], v[98:99]
	v_mov_b64_e32 v[76:77], v[98:99]
	v_mov_b64_e32 v[78:79], v[98:99]
	v_mov_b64_e32 v[80:81], v[98:99]
	v_mov_b64_e32 v[82:83], v[98:99]
	v_mov_b64_e32 v[84:85], v[98:99]
	v_mov_b64_e32 v[86:87], v[98:99]
	v_mov_b64_e32 v[88:89], v[98:99]
	v_mov_b64_e32 v[90:91], v[98:99]
	v_mov_b64_e32 v[92:93], v[98:99]
	v_mov_b64_e32 v[94:95], v[98:99]
	v_mov_b64_e32 v[96:97], v[98:99]
	v_mov_b64_e32 v[100:101], v[98:99]
	v_mov_b64_e32 v[102:103], v[98:99]
	v_mov_b64_e32 v[104:105], v[98:99]
	v_mov_b64_e32 v[106:107], v[98:99]
	v_mov_b64_e32 v[108:109], v[98:99]
	v_mov_b64_e32 v[110:111], v[98:99]
	v_mov_b64_e32 v[112:113], v[98:99]
	v_mov_b64_e32 v[114:115], v[98:99]
	v_mov_b64_e32 v[116:117], v[98:99]
	v_mov_b64_e32 v[118:119], v[98:99]
	v_mov_b64_e32 v[120:121], v[98:99]
	v_mov_b64_e32 v[122:123], v[98:99]
	v_mov_b64_e32 v[124:125], v[98:99]
	v_mov_b64_e32 v[126:127], v[98:99]
	v_mov_b64_e32 v[128:129], v[98:99]
	v_mov_b64_e32 v[130:131], v[98:99]
	v_mov_b64_e32 v[132:133], v[98:99]
	v_mov_b64_e32 v[134:135], v[98:99]
	v_mov_b64_e32 v[136:137], v[98:99]
	v_mov_b64_e32 v[138:139], v[98:99]
	v_mov_b64_e32 v[140:141], v[98:99]
	v_mov_b64_e32 v[142:143], v[98:99]
	v_mov_b64_e32 v[144:145], v[98:99]
	v_mov_b64_e32 v[146:147], v[98:99]
	v_mov_b64_e32 v[148:149], v[98:99]
	v_mov_b64_e32 v[150:151], v[98:99]
	v_mov_b64_e32 v[152:153], v[98:99]
	v_mov_b64_e32 v[154:155], v[98:99]
	v_mov_b64_e32 v[156:157], v[98:99]
	v_mov_b64_e32 v[158:159], v[98:99]
	v_mov_b64_e32 v[160:161], v[98:99]
	v_mov_b64_e32 v[162:163], v[98:99]
	v_mov_b64_e32 v[164:165], v[98:99]
	v_mov_b64_e32 v[166:167], v[98:99]
	v_mov_b64_e32 v[168:169], v[98:99]
	v_mov_b64_e32 v[170:171], v[98:99]
	v_mov_b64_e32 v[172:173], v[98:99]
	v_mov_b64_e32 v[174:175], v[98:99]
	v_mov_b64_e32 v[176:177], v[98:99]
	v_mov_b64_e32 v[178:179], v[98:99]
	v_mov_b64_e32 v[180:181], v[98:99]
	v_mov_b64_e32 v[182:183], v[98:99]
	v_mov_b64_e32 v[184:185], v[98:99]
	v_mov_b64_e32 v[186:187], v[98:99]
	v_mov_b64_e32 v[188:189], v[98:99]
	v_mov_b64_e32 v[190:191], v[98:99]
	v_mov_b64_e32 v[192:193], v[98:99]
	s_branch .LBB0_624

;     ...
; #pragma unroll
;         for (int a = 0; a < 2; ++a)
; #pragma unroll
;             for (int b = 0; b < 2; ++b)
; #pragma unroll
;                 for (int m = 0; m < 4; ++m)
; #pragma unroll
;                     for (int n = 0; n < 2; ++n) acc[a][b][m][n] = (f32x4){0.f, 0.f, 0.f, 0.f};
;         cur = nxt; cA = nA; cB = nB; ++ui; relax = ALIGN_EPI;
.LBB0_793:
	s_add_u32 s48, s2, 0x80000
	s_addc_u32 s49, s3, 0
	s_add_u32 s2, s4, 0x80
	s_addc_u32 s3, s5, 0
	v_mov_b32_e32 v74, 0
	v_lshl_add_u64 v[210:211], s[2:3], 0, v[206:207]
	v_lshl_add_u64 v[212:213], s[2:3], 0, v[208:209]
	s_mov_b32 s50, -2
	s_mov_b64 s[14:15], 0
	v_mov_b32_e32 v75, v74
	v_mov_b64_e32 v[66:67], v[74:75]
	v_mov_b64_e32 v[68:69], v[74:75]
	v_mov_b64_e32 v[70:71], v[74:75]
	v_mov_b64_e32 v[72:73], v[74:75]
	v_mov_b64_e32 v[76:77], v[74:75]
	v_mov_b64_e32 v[78:79], v[74:75]
	v_mov_b64_e32 v[80:81], v[74:75]
	v_mov_b64_e32 v[82:83], v[74:75]
	v_mov_b64_e32 v[84:85], v[74:75]
	v_mov_b64_e32 v[86:87], v[74:75]
	v_mov_b64_e32 v[88:89], v[74:75]
	v_mov_b64_e32 v[90:91], v[74:75]
	v_mov_b64_e32 v[92:93], v[74:75]
	v_mov_b64_e32 v[94:95], v[74:75]
	v_mov_b64_e32 v[96:97], v[74:75]
	v_mov_b64_e32 v[98:99], v[74:75]
	v_mov_b64_e32 v[100:101], v[74:75]
	v_mov_b64_e32 v[102:103], v[74:75]
	v_mov_b64_e32 v[104:105], v[74:75]
	v_mov_b64_e32 v[106:107], v[74:75]
	v_mov_b64_e32 v[108:109], v[74:75]
	v_mov_b64_e32 v[110:111], v[74:75]
	v_mov_b64_e32 v[112:113], v[74:75]
	v_mov_b64_e32 v[114:115], v[74:75]
	v_mov_b64_e32 v[116:117], v[74:75]
	v_mov_b64_e32 v[118:119], v[74:75]
	v_mov_b64_e32 v[120:121], v[74:75]
	v_mov_b64_e32 v[122:123], v[74:75]
	v_mov_b64_e32 v[124:125], v[74:75]
	v_mov_b64_e32 v[126:127], v[74:75]
	v_mov_b64_e32 v[128:129], v[74:75]
	v_mov_b64_e32 v[130:131], v[74:75]
	v_mov_b64_e32 v[132:133], v[74:75]
	v_mov_b64_e32 v[134:135], v[74:75]
	v_mov_b64_e32 v[136:137], v[74:75]
	v_mov_b64_e32 v[138:139], v[74:75]
	v_mov_b64_e32 v[140:141], v[74:75]
	v_mov_b64_e32 v[142:143], v[74:75]
	v_mov_b64_e32 v[144:145], v[74:75]
	v_mov_b64_e32 v[146:147], v[74:75]
	v_mov_b64_e32 v[148:149], v[74:75]
	v_mov_b64_e32 v[150:151], v[74:75]
	v_mov_b64_e32 v[152:153], v[74:75]
	v_mov_b64_e32 v[154:155], v[74:75]
	v_mov_b64_e32 v[156:157], v[74:75]
	v_mov_b64_e32 v[158:159], v[74:75]
	v_mov_b64_e32 v[160:161], v[74:75]
	v_mov_b64_e32 v[162:163], v[74:75]
	v_mov_b64_e32 v[164:165], v[74:75]
	v_mov_b64_e32 v[166:167], v[74:75]
	v_mov_b64_e32 v[168:169], v[74:75]
	v_mov_b64_e32 v[170:171], v[74:75]
	v_mov_b64_e32 v[172:173], v[74:75]
	v_mov_b64_e32 v[174:175], v[74:75]
	v_mov_b64_e32 v[176:177], v[74:75]
	v_mov_b64_e32 v[178:179], v[74:75]
	v_mov_b64_e32 v[180:181], v[74:75]
	v_mov_b64_e32 v[182:183], v[74:75]
	v_mov_b64_e32 v[184:185], v[74:75]
	v_mov_b64_e32 v[186:187], v[74:75]
	v_mov_b64_e32 v[188:189], v[74:75]
	v_mov_b64_e32 v[190:191], v[74:75]
	v_mov_b64_e32 v[192:193], v[74:75]
	s_branch .LBB0_795

;     ...
; #pragma unroll
;         for (int a = 0; a < 2; ++a)
; #pragma unroll
;             for (int b = 0; b < 2; ++b)
; #pragma unroll
;                 for (int m = 0; m < 4; ++m)
; #pragma unroll
;                     for (int n = 0; n < 2; ++n) acc[a][b][m][n] = (f32x4){0.f, 0.f, 0.f, 0.f};
;         cur = nxt; cA = nA; cB = nB; ++ui; relax = ALIGN_EPI;
.LBB0_1297:
	s_add_u32 s49, s4, 0x40000
	s_addc_u32 s50, s5, 0
	s_add_u32 s4, s16, 0x80
	v_mov_b32_e32 v209, v65
	v_mov_b32_e32 v211, v65
	s_addc_u32 s5, s17, 0
	v_mov_b32_e32 v66, 0
	v_lshl_add_u64 v[212:213], s[4:5], 0, v[210:211]
	v_lshl_add_u64 v[214:215], s[4:5], 0, v[208:209]
	s_mov_b32 s51, -2
	s_mov_b64 s[20:21], 0
	v_mov_b32_e32 v67, v66
	v_mov_b64_e32 v[68:69], v[66:67]
	v_mov_b64_e32 v[70:71], v[66:67]
	v_mov_b64_e32 v[72:73], v[66:67]
	v_mov_b64_e32 v[74:75], v[66:67]
	v_mov_b64_e32 v[76:77], v[66:67]
	v_mov_b64_e32 v[78:79], v[66:67]
	v_mov_b64_e32 v[80:81], v[66:67]
	v_mov_b64_e32 v[82:83], v[66:67]
	v_mov_b64_e32 v[84:85], v[66:67]
	v_mov_b64_e32 v[86:87], v[66:67]
	v_mov_b64_e32 v[88:89], v[66:67]
	v_mov_b64_e32 v[90:91], v[66:67]
	v_mov_b64_e32 v[92:93], v[66:67]
	v_mov_b64_e32 v[94:95], v[66:67]
	v_mov_b64_e32 v[96:97], v[66:67]
	v_mov_b64_e32 v[98:99], v[66:67]
	v_mov_b64_e32 v[100:101], v[66:67]
	v_mov_b64_e32 v[102:103], v[66:67]
	v_mov_b64_e32 v[104:105], v[66:67]
	v_mov_b64_e32 v[106:107], v[66:67]
	v_mov_b64_e32 v[108:109], v[66:67]
	v_mov_b64_e32 v[110:111], v[66:67]
	v_mov_b64_e32 v[112:113], v[66:67]
	v_mov_b64_e32 v[114:115], v[66:67]
	v_mov_b64_e32 v[116:117], v[66:67]
	v_mov_b64_e32 v[118:119], v[66:67]
	v_mov_b64_e32 v[120:121], v[66:67]
	v_mov_b64_e32 v[122:123], v[66:67]
	v_mov_b64_e32 v[124:125], v[66:67]
	v_mov_b64_e32 v[126:127], v[66:67]
	v_mov_b64_e32 v[128:129], v[66:67]
	v_mov_b64_e32 v[130:131], v[66:67]
	v_mov_b64_e32 v[132:133], v[66:67]
	v_mov_b64_e32 v[134:135], v[66:67]
	v_mov_b64_e32 v[136:137], v[66:67]
	v_mov_b64_e32 v[138:139], v[66:67]
	v_mov_b64_e32 v[140:141], v[66:67]
	v_mov_b64_e32 v[142:143], v[66:67]
	v_mov_b64_e32 v[144:145], v[66:67]
	v_mov_b64_e32 v[146:147], v[66:67]
	v_mov_b64_e32 v[148:149], v[66:67]
	v_mov_b64_e32 v[150:151], v[66:67]
	v_mov_b64_e32 v[152:153], v[66:67]
	v_mov_b64_e32 v[154:155], v[66:67]
	v_mov_b64_e32 v[156:157], v[66:67]
	v_mov_b64_e32 v[158:159], v[66:67]
	v_mov_b64_e32 v[160:161], v[66:67]
	v_mov_b64_e32 v[162:163], v[66:67]
	v_mov_b64_e32 v[164:165], v[66:67]
	v_mov_b64_e32 v[166:167], v[66:67]
	v_mov_b64_e32 v[168:169], v[66:67]
	v_mov_b64_e32 v[170:171], v[66:67]
	v_mov_b64_e32 v[172:173], v[66:67]
	v_mov_b64_e32 v[174:175], v[66:67]
	v_mov_b64_e32 v[176:177], v[66:67]
	v_mov_b64_e32 v[178:179], v[66:67]
	v_mov_b64_e32 v[180:181], v[66:67]
	v_mov_b64_e32 v[182:183], v[66:67]
	v_mov_b64_e32 v[184:185], v[66:67]
	v_mov_b64_e32 v[186:187], v[66:67]
	v_mov_b64_e32 v[188:189], v[66:67]
	v_mov_b64_e32 v[190:191], v[66:67]
	v_mov_b64_e32 v[192:193], v[66:67]
	s_branch .LBB0_1299

;     ...
; #pragma unroll
;         for (int a = 0; a < 2; ++a)
; #pragma unroll
;             for (int b = 0; b < 2; ++b)
; #pragma unroll
;                 for (int m = 0; m < 4; ++m)
; #pragma unroll
;                     for (int n = 0; n < 2; ++n) acc[a][b][m][n] = (f32x4){0.f, 0.f, 0.f, 0.f};
;         cur = nxt; cA = nA; cB = nB; ++ui; relax = ALIGN_EPI;
.LBB0_1409:
	v_mov_b32_e32 v86, 0
	s_mov_b32 s5, 0
	s_mov_b64 s[22:23], -1
	s_mov_b64 s[2:3], 0
	v_mov_b32_e32 v87, v86
	v_mov_b64_e32 v[66:67], v[86:87]
	v_mov_b64_e32 v[68:69], v[86:87]
	v_mov_b64_e32 v[70:71], v[86:87]
	v_mov_b64_e32 v[72:73], v[86:87]
	v_mov_b64_e32 v[74:75], v[86:87]
	v_mov_b64_e32 v[76:77], v[86:87]
	v_mov_b64_e32 v[78:79], v[86:87]
	v_mov_b64_e32 v[80:81], v[86:87]
	v_mov_b64_e32 v[82:83], v[86:87]
	v_mov_b64_e32 v[84:85], v[86:87]
	v_mov_b64_e32 v[88:89], v[86:87]
	v_mov_b64_e32 v[90:91], v[86:87]
	v_mov_b64_e32 v[92:93], v[86:87]
	v_mov_b64_e32 v[94:95], v[86:87]
	v_mov_b64_e32 v[96:97], v[86:87]
	v_mov_b64_e32 v[98:99], v[86:87]
	v_mov_b64_e32 v[100:101], v[86:87]
	v_mov_b64_e32 v[102:103], v[86:87]
	v_mov_b64_e32 v[104:105], v[86:87]
	v_mov_b64_e32 v[106:107], v[86:87]
	v_mov_b64_e32 v[108:109], v[86:87]
	v_mov_b64_e32 v[110:111], v[86:87]
	v_mov_b64_e32 v[112:113], v[86:87]
	v_mov_b64_e32 v[114:115], v[86:87]
	v_mov_b64_e32 v[116:117], v[86:87]
	v_mov_b64_e32 v[118:119], v[86:87]
	v_mov_b64_e32 v[120:121], v[86:87]
	v_mov_b64_e32 v[122:123], v[86:87]
	v_mov_b64_e32 v[124:125], v[86:87]
	v_mov_b64_e32 v[126:127], v[86:87]
	v_mov_b64_e32 v[128:129], v[86:87]
	v_mov_b64_e32 v[130:131], v[86:87]
	v_mov_b64_e32 v[132:133], v[86:87]
	v_mov_b64_e32 v[134:135], v[86:87]
	v_mov_b64_e32 v[136:137], v[86:87]
	v_mov_b64_e32 v[138:139], v[86:87]
	v_mov_b64_e32 v[140:141], v[86:87]
	v_mov_b64_e32 v[142:143], v[86:87]
	v_mov_b64_e32 v[144:145], v[86:87]
	v_mov_b64_e32 v[146:147], v[86:87]
	v_mov_b64_e32 v[148:149], v[86:87]
	v_mov_b64_e32 v[150:151], v[86:87]
	v_mov_b64_e32 v[152:153], v[86:87]
	v_mov_b64_e32 v[154:155], v[86:87]
	v_mov_b64_e32 v[156:157], v[86:87]
	v_mov_b64_e32 v[158:159], v[86:87]
	v_mov_b64_e32 v[160:161], v[86:87]
	v_mov_b64_e32 v[162:163], v[86:87]
	v_mov_b64_e32 v[164:165], v[86:87]
	v_mov_b64_e32 v[166:167], v[86:87]
	v_mov_b64_e32 v[168:169], v[86:87]
	v_mov_b64_e32 v[170:171], v[86:87]
	v_mov_b64_e32 v[172:173], v[86:87]
	v_mov_b64_e32 v[174:175], v[86:87]
	v_mov_b64_e32 v[176:177], v[86:87]
	v_mov_b64_e32 v[178:179], v[86:87]
	v_mov_b64_e32 v[180:181], v[86:87]
	v_mov_b64_e32 v[182:183], v[86:87]
	v_mov_b64_e32 v[184:185], v[86:87]
	v_mov_b64_e32 v[186:187], v[86:87]
	v_mov_b64_e32 v[188:189], v[86:87]
	v_mov_b64_e32 v[190:191], v[86:87]
	v_mov_b64_e32 v[192:193], v[86:87]
	s_branch .LBB0_1411
